# mLSTM Seg B: S fragment reads issued before the V staging arithmetic; Q.C state conversions + first 6 Q fragment reads issued before the W (masked exp) arithmetic
# baseline (speedup 1.0000x reference)
.LBB0_730:
	s_waitcnt lgkmcnt(0)
	s_barrier
	ds_read_b32 v0, v124 offset:1024
	ds_read_b128 v[222:225], v162
	ds_read_b128 v[226:229], v163 offset:33792
	ds_read_b128 v[84:87], v163 offset:42240
	ds_read_b128 v[210:213], v162 offset:64
	ds_read_b128 v[214:217], v163 offset:33856
	ds_read_b128 v[218:221], v163 offset:42304
	ds_read_b128 v[232:235], v162 offset:128
	ds_read_b128 v[236:239], v163 offset:33920
	ds_read_b128 v[240:243], v163 offset:42368
	ds_read_b128 v[176:179], v162 offset:192
	ds_read_b128 v[180:183], v163 offset:33984
	ds_read_b128 v[184:187], v163 offset:42432
	v_add_u32_e32 v167, 0x4000, v165
	v_add_u32_e32 v168, 0x6000, v165
	v_lshlrev_b32_e32 v72, 16, v36
	v_and_b32_e32 v73, 0xffff0000, v36
	ds_write_b128 v142, v[36:39]
	v_and_b32_e32 v74, 0xffff0000, v37
	s_waitcnt lgkmcnt(13)
	v_mul_f32_e32 v72, v0, v72
	v_mul_f32_e32 v73, v0, v73
	v_cvt_pk_bf16_f32 v72, v72, v73
	v_lshlrev_b32_e32 v73, 16, v37
	v_mul_f32_e32 v73, v0, v73
	v_mul_f32_e32 v74, v0, v74
	v_cvt_pk_bf16_f32 v73, v73, v74
	v_lshlrev_b32_e32 v74, 16, v38
	v_and_b32_e32 v75, 0xffff0000, v38
	v_mul_f32_e32 v74, v0, v74
	v_mul_f32_e32 v75, v0, v75
	v_cvt_pk_bf16_f32 v74, v74, v75
	v_lshlrev_b32_e32 v75, 16, v39
	v_mul_f32_e32 v75, v0, v75
	v_and_b32_e32 v76, 0xffff0000, v39
	v_mul_f32_e32 v0, v0, v76
	v_cvt_pk_bf16_f32 v75, v75, v0
	ds_write_b128 v143, v[72:75]
	s_cmp_eq_u32 s88, 0x3e0000
	s_cbranch_scc1 .Lml_no_v_fetch
	v_mov_b32_e32 v36, v118
	s_nop 0
	global_load_dwordx4 v[36:39], v36, s[92:93]
.Lml_no_v_fetch:
	s_waitcnt lgkmcnt(2)
	v_mfma_f32_16x16x32_bf16 v[76:79], v[222:225], v[226:229], 0
	v_mfma_f32_16x16x32_bf16 v[72:75], v[222:225], v[84:87], 0
	ds_read_b128 v[194:197], v162 offset:256
	ds_read_b128 v[198:201], v163 offset:34048
	ds_read_b128 v[202:205], v163 offset:42496
	v_mfma_f32_16x16x32_bf16 v[76:79], v[210:213], v[214:217], v[76:79]
	v_mfma_f32_16x16x32_bf16 v[72:75], v[210:213], v[218:221], v[72:75]
	ds_read_b128 v[210:213], v162 offset:320
	ds_read_b128 v[214:217], v163 offset:34112
	ds_read_b128 v[218:221], v163 offset:42560
	v_mfma_f32_16x16x32_bf16 v[76:79], v[232:235], v[236:239], v[76:79]
	v_mfma_f32_16x16x32_bf16 v[72:75], v[232:235], v[240:243], v[72:75]
	ds_read_b128 v[232:235], v162 offset:384
	ds_read_b128 v[236:239], v163 offset:34176
	ds_read_b128 v[240:243], v163 offset:42624
	v_mfma_f32_16x16x32_bf16 v[76:79], v[176:179], v[180:183], v[76:79]
	v_mfma_f32_16x16x32_bf16 v[72:75], v[176:179], v[184:187], v[72:75]
	ds_read_b128 v[176:179], v162 offset:448
	ds_read_b128 v[180:183], v163 offset:34240
	ds_read_b128 v[184:187], v163 offset:42688
	ds_read_b128 v[80:83], v150
	ds_read_b32 v0, v151
	ds_read_b32 v84, v164 offset:64
	s_waitcnt lgkmcnt(13)
	v_mfma_f32_16x16x32_bf16 v[76:79], v[194:197], v[198:201], v[76:79]
	s_waitcnt lgkmcnt(12)
	v_mfma_f32_16x16x32_bf16 v[72:75], v[194:197], v[202:205], v[72:75]
	s_waitcnt lgkmcnt(10)
	v_mfma_f32_16x16x32_bf16 v[76:79], v[210:213], v[214:217], v[76:79]
	s_waitcnt lgkmcnt(9)
	v_mfma_f32_16x16x32_bf16 v[72:75], v[210:213], v[218:221], v[72:75]
	s_waitcnt lgkmcnt(7)
	v_mfma_f32_16x16x32_bf16 v[76:79], v[232:235], v[236:239], v[76:79]
	s_waitcnt lgkmcnt(6)
	v_mfma_f32_16x16x32_bf16 v[72:75], v[232:235], v[240:243], v[72:75]
	s_waitcnt lgkmcnt(4)
	v_mfma_f32_16x16x32_bf16 v[76:79], v[176:179], v[180:183], v[76:79]
	s_waitcnt lgkmcnt(3)
	v_mfma_f32_16x16x32_bf16 v[72:75], v[176:179], v[184:187], v[72:75]
	s_nop 3
	v_add_u32_e32 v92, 0x2000, v165
	v_cvt_pk_bf16_f32 v244, v68, v69
	v_cvt_pk_bf16_f32 v245, v70, v71
	v_cvt_pk_bf16_f32 v246, v64, v65
	v_cvt_pk_bf16_f32 v247, v66, v67
	v_cvt_pk_bf16_f32 v206, v56, v57
	v_cvt_pk_bf16_f32 v207, v58, v59
	v_cvt_pk_bf16_f32 v208, v60, v61
	v_cvt_pk_bf16_f32 v209, v62, v63
	v_cvt_pk_bf16_f32 v222, v48, v49
	v_cvt_pk_bf16_f32 v223, v50, v51
	v_cvt_pk_bf16_f32 v224, v52, v53
	v_cvt_pk_bf16_f32 v225, v54, v55
	v_cvt_pk_bf16_f32 v226, v40, v41
	v_cvt_pk_bf16_f32 v227, v42, v43
	v_cvt_pk_bf16_f32 v228, v44, v45
	v_cvt_pk_bf16_f32 v229, v46, v47
	ds_read_b64 v[210:211], v165
	ds_read_b64 v[212:213], v165 offset:32
	ds_read_b64 v[214:215], v92 offset:256
	ds_read_b64 v[216:217], v92 offset:288
	ds_read_b64 v[218:219], v167 offset:512
	ds_read_b64 v[220:221], v167 offset:544
	ds_read_b64 v[232:233], v168 offset:768
	ds_read_b64 v[234:235], v168 offset:800
	ds_read_b64 v[236:237], v165 offset:64
	ds_read_b64 v[238:239], v165 offset:96
	ds_read_b64 v[240:241], v92 offset:320
	ds_read_b64 v[242:243], v92 offset:352
	s_waitcnt lgkmcnt(13)
	v_sub_f32_e32 v85, v0, v80
	v_min_f32_e32 v85, 0, v85
	s_waitcnt lgkmcnt(12)
	v_sub_f32_e32 v80, v84, v80
	v_exp_f32_e32 v85, v85
	v_min_f32_e32 v80, 0, v80
	v_exp_f32_e32 v80, v80
	v_mul_f32_e32 v76, v76, v85
	v_cndmask_b32_e64 v76, v76, 0, s[64:65]
	v_mul_f32_e32 v72, v72, v80
	v_cndmask_b32_e64 v72, v72, 0, s[66:67]
	v_cvt_pk_bf16_f32 v76, v76, v1
	v_add_u32_e32 v80, v155, v152
	ds_write_b16 v80, v76
	v_cvt_pk_bf16_f32 v72, v72, v1
	v_add_u32_e32 v76, v155, v153
	ds_write_b16 v76, v72
	v_sub_f32_e32 v72, v0, v81
	v_min_f32_e32 v72, 0, v72
	v_sub_f32_e32 v76, v84, v81
	v_exp_f32_e32 v72, v72
	v_min_f32_e32 v76, 0, v76
	v_exp_f32_e32 v76, v76
	v_mul_f32_e32 v72, v77, v72
	v_cndmask_b32_e64 v72, v72, 0, s[68:69]
	v_mul_f32_e32 v73, v73, v76
	v_cndmask_b32_e64 v73, v73, 0, s[70:71]
	v_cvt_pk_bf16_f32 v72, v72, v1
	v_add_u32_e32 v76, v156, v152
	ds_write_b16 v76, v72
	v_cvt_pk_bf16_f32 v72, v73, v1
	v_add_u32_e32 v73, v156, v153
	ds_write_b16 v73, v72
	v_sub_f32_e32 v72, v0, v82
	v_min_f32_e32 v72, 0, v72
	v_sub_f32_e32 v73, v84, v82
	v_exp_f32_e32 v72, v72
	v_min_f32_e32 v73, 0, v73
	v_exp_f32_e32 v73, v73
	v_sub_f32_e32 v0, v0, v83
	v_mul_f32_e32 v72, v78, v72
	v_cndmask_b32_e64 v72, v72, 0, s[72:73]
	v_mul_f32_e32 v73, v74, v73
	v_cndmask_b32_e64 v73, v73, 0, s[74:75]
	v_cvt_pk_bf16_f32 v72, v72, v1
	v_add_u32_e32 v74, v157, v152
	ds_write_b16 v74, v72
	v_cvt_pk_bf16_f32 v72, v73, v1
	v_add_u32_e32 v73, v157, v153
	ds_write_b16 v73, v72
	v_min_f32_e32 v0, 0, v0
	v_sub_f32_e32 v72, v84, v83
	v_exp_f32_e32 v0, v0
	v_min_f32_e32 v72, 0, v72
	v_exp_f32_e32 v72, v72
	v_add_u32_e32 v73, v158, v152
	v_mul_f32_e32 v0, v79, v0
	v_cndmask_b32_e64 v0, v0, 0, s[76:77]
	v_mul_f32_e32 v72, v75, v72
	v_cndmask_b32_e64 v72, v72, 0, s[78:79]
	v_cvt_pk_bf16_f32 v0, v0, v1
	ds_write_b16 v73, v0
	v_cvt_pk_bf16_f32 v0, v72, v1
	v_add_u32_e32 v72, v158, v153
	ds_write_b16 v72, v0
	v_add_u32_e32 v0, 0x2000, v165
	s_waitcnt lgkmcnt(8)
	ds_read_b64 v[176:177], v167 offset:576
	ds_read_b64 v[178:179], v167 offset:608
	ds_read_b64 v[180:181], v168 offset:832
	ds_read_b64 v[182:183], v168 offset:864
	ds_read_b64 v[184:185], v165 offset:128
	ds_read_b64 v[186:187], v165 offset:160
	ds_read_b64 v[194:195], v0 offset:384
	ds_read_b64 v[196:197], v0 offset:416
	ds_read_b64 v[198:199], v167 offset:640
	ds_read_b64 v[200:201], v167 offset:672
	ds_read_b64 v[202:203], v168 offset:896
	ds_read_b64 v[204:205], v168 offset:928
	v_mfma_f32_16x16x32_bf16 v[76:79], v[210:213], v[244:247], 0
	v_mfma_f32_16x16x32_bf16 v[80:83], v[214:217], v[244:247], 0
	v_mfma_f32_16x16x32_bf16 v[84:87], v[218:221], v[244:247], 0
	v_mfma_f32_16x16x32_bf16 v[88:91], v[232:235], v[244:247], 0
	v_mfma_f32_16x16x32_bf16 v[76:79], v[236:239], v[206:209], v[76:79]
	v_mfma_f32_16x16x32_bf16 v[80:83], v[240:243], v[206:209], v[80:83]
	s_waitcnt lgkmcnt(10)
	v_mfma_f32_16x16x32_bf16 v[84:87], v[176:179], v[206:209], v[84:87]
	ds_read_b64 v[210:211], v165 offset:192
	ds_read_b64 v[212:213], v165 offset:224
	s_waitcnt lgkmcnt(10)
	v_mfma_f32_16x16x32_bf16 v[88:91], v[180:183], v[206:209], v[88:91]
	ds_read_b64 v[214:215], v0 offset:448
	ds_read_b64 v[216:217], v0 offset:480
	s_waitcnt lgkmcnt(10)
	v_mfma_f32_16x16x32_bf16 v[76:79], v[184:187], v[222:225], v[76:79]
	ds_read_b64 v[218:219], v167 offset:704
	ds_read_b64 v[220:221], v167 offset:736
	s_waitcnt lgkmcnt(10)
	v_mfma_f32_16x16x32_bf16 v[80:83], v[194:197], v[222:225], v[80:83]
	ds_read_b64 v[232:233], v168 offset:960
	ds_read_b64 v[234:235], v168 offset:992
	s_waitcnt lgkmcnt(10)
	v_mfma_f32_16x16x32_bf16 v[84:87], v[198:201], v[222:225], v[84:87]
	s_waitcnt lgkmcnt(8)
	v_mfma_f32_16x16x32_bf16 v[88:91], v[202:205], v[222:225], v[88:91]
	s_waitcnt lgkmcnt(6)
	v_mfma_f32_16x16x32_bf16 v[76:79], v[210:213], v[226:229], v[76:79]
	s_waitcnt lgkmcnt(4)
	v_mfma_f32_16x16x32_bf16 v[80:83], v[214:217], v[226:229], v[80:83]
	s_waitcnt lgkmcnt(2)
	v_mfma_f32_16x16x32_bf16 v[84:87], v[218:221], v[226:229], v[84:87]
	s_waitcnt lgkmcnt(0)
	s_barrier
	v_mfma_f32_16x16x32_bf16 v[88:91], v[232:235], v[226:229], v[88:91]
